# in-projection unit boundaries carry one more weight-conversion slice (second register set), stand-alone conversion stages lose 3 experts
# speedup vs baseline: 1.0118x; 1.0025x over previous
.LBB0_215:
	s_cmp_lt_i32 s4, 3
	s_waitcnt lgkmcnt(0)
	s_cselect_b64 s[0:1], -1, 0
	s_cmp_gt_i32 s5, 2
	s_cselect_b64 s[2:3], -1, 0
	s_and_b64 s[0:1], s[0:1], s[2:3]
	s_andn2_b64 vcc, exec, s[0:1]
	s_cbranch_vccnz .LBB0_347
	v_readlane_b32 s18, v254, 11
	s_load_dword s6, s[52:53], 0xd0
	s_load_dwordx2 s[4:5], s[52:53], 0xc0
	s_bitcmp0_b32 s18, 0
	s_cselect_b64 s[0:1], -1, 0
	s_bitcmp1_b32 s18, 0
	v_readlane_b32 s8, v254, 10
	s_cselect_b64 s[10:11], -1, 0
	s_lshl_b32 s2, s8, 14
	s_add_i32 s36, s2, 0
	s_lshl_b32 s2, s18, 2
	s_add_i32 s37, s2, s8
	s_waitcnt lgkmcnt(0)
	s_lshl_b32 s2, s6, 2
	s_add_i32 s2, s2, 4
	s_and_b32 s38, s2, -8
	s_cmpk_lt_i32 s37, 0x1400
	s_cselect_b64 s[2:3], -1, 0
	s_add_u32 s39, s4, 0x2000000
	s_addc_u32 s40, s5, 0
	s_lshl_b32 s4, s18, 3
	s_add_i32 s57, s8, s4
	s_lshl_b32 s41, s6, 3
	s_addk_i32 s57, 0x1400
	s_movk_i32 s32, 0x4c00
	s_cmpk_eq_i32 s99, 0x100
	s_cselect_b32 s32, 0x4000, s32
	s_cmp_lt_i32 s57, s32
	s_cselect_b64 s[14:15], -1, 0
	s_lshl_b32 s4, s50, 3
	s_bfe_u32 s6, s61, 0x20006
	s_lshr_b32 s7, s61, 8
	s_add_i32 s59, s8, s4
	s_add_i32 s5, s41, 0x2fff
	s_mov_b32 s20, s61
	s_lshl_b32 s61, s8, 10
	s_lshl_b32 s63, s7, 6
	s_lshl_b32 s65, s7, 13
	s_lshl_b32 s67, s6, 12
	s_cmpk_lt_i32 s18, 0x600
	s_cselect_b64 s[16:17], -1, 0
	s_ashr_i32 s4, s18, 31
	s_lshr_b32 s4, s4, 29
	s_add_i32 s4, s18, s4
	s_ashr_i32 s8, s4, 3
	s_and_b32 s4, s4, -8
	s_sub_i32 s4, s18, s4
	s_cmp_lt_i32 s4, 0
	s_movk_i32 s69, 0xc1
	s_cselect_b32 s18, s69, 0xc0
	s_mul_i32 s4, s18, s4
	s_add_i32 s4, s4, s8
	s_mul_hi_i32 s8, s4, 0x2aaaaaab
	s_lshr_b32 s18, s8, 31
	s_ashr_i32 s8, s8, 4
	s_add_i32 s8, s8, s18
	s_lshl_b32 s82, s8, 3
	s_mulk_i32 s8, 0x60
	s_sub_i32 s8, s4, s8
	s_bfe_i32 s4, s8, 0x80000
	s_bfe_u32 s4, s4, 0x3000c
	s_add_i32 s18, s8, s4
	s_bfe_i32 s4, s18, 0x80000
	s_and_b32 s18, s18, 0xf8
	s_sub_i32 s8, s8, s18
	s_sext_i32_i16 s19, s4
	s_sext_i32_i8 s8, s8
	s_lshr_b32 s4, s19, 3
	s_add_i32 s82, s82, s8
	s_ashr_i32 s44, s19, 3
	s_cmp_eq_u32 s7, 1
	s_cselect_b64 s[18:19], -1, 0
	s_cmpk_lt_u32 s20, 0x100
	s_cselect_b64 s[20:21], -1, 0
	s_and_b64 s[22:23], s[0:1], s[2:3]
	s_abs_i32 s2, s41
	v_cvt_f32_u32_e32 v0, s2
	s_bfe_i64 s[0:1], s[4:5], 0x100000
	s_sub_i32 s3, 0, s2
	s_lshl_b64 s[26:27], s[0:1], 20
	v_rcp_iflag_f32_e32 v0, v0
	s_abs_i32 s1, s5
	s_lshl_b32 s86, s82, 8
	s_xor_b32 s0, s5, s41
	v_mul_f32_e32 v0, 0x4f7ffffe, v0
	v_cvt_u32_f32_e32 v0, v0
	s_lshl_b32 s84, s6, 6
	s_lshl_b32 s85, s82, 20
	s_bitset1_b32 s86, 7
	v_readfirstlane_b32 s4, v0
	s_mul_i32 s3, s3, s4
	s_mul_hi_u32 s3, s4, s3
	s_add_i32 s4, s4, s3
	s_mul_hi_u32 s3, s1, s4
	s_mul_i32 s4, s3, s2
	s_sub_i32 s1, s1, s4
	s_ashr_i32 s0, s0, 31
	s_add_i32 s4, s3, 1
	s_sub_i32 s5, s1, s2
	s_cmp_ge_u32 s1, s2
	s_cselect_b32 s3, s4, s3
	s_cselect_b32 s1, s5, s1
	s_add_i32 s4, s3, 1
	s_cmp_ge_u32 s1, s2
	s_cselect_b32 s1, s4, s3
	s_xor_b32 s1, s1, s0
	s_sub_i32 s87, s1, s0
	s_mov_b32 s9, 0
	s_mov_b64 s[12:13], 0x2000000
	s_add_i32 s88, s87, -1
	v_mov_b32_e32 v161, 0
	s_movk_i32 s89, 0x104
	s_movk_i32 s90, 0x4000
	s_mov_b32 s91, 0x8000
	s_mov_b32 s92, 0xc000
	s_mov_b32 s93, 0x10000
	s_mov_b64 s[52:53], 0x80
	s_mov_b64 s[54:55], 0x32000080
	s_mov_b32 s56, 0x3e6d3388
	s_mov_b32 s58, 0x3f07dc22
	s_mov_b32 s60, 0xbf3a00e3
	s_mov_b32 s62, 0x3f35f0e3
	s_mov_b32 s64, 0xbe11a98e
	s_mov_b32 s66, 0x3e027906
	s_mov_b32 s68, 0xbf38aa3b
	s_movk_i32 s94, 0x1800
	s_mov_b32 s95, 0x2001000
	v_mov_b32_e32 v176, 1
	s_mov_b32 s96, 0
	s_branch .LBB0_218

.LBB0_228:
	v_add_u32_e32 v22, s2, v26
	v_ashrrev_i32_e32 v23, 4, v22
	v_ashrrev_i32_e32 v27, 3, v22
	v_add_u32_e32 v28, 64, v22
	v_add_u32_e32 v29, 0x80, v22
	v_add_u32_e32 v22, 0xc0, v22
	v_and_b32_e32 v30, 7, v23
	v_ashrrev_i32_e32 v32, 4, v28
	v_ashrrev_i32_e32 v33, 3, v28
	v_ashrrev_i32_e32 v28, 4, v29
	v_ashrrev_i32_e32 v36, 3, v29
	v_ashrrev_i32_e32 v29, 4, v22
	v_mad_u64_u32 v[24:25], s[6:7], v23, s89, v[18:19]
	v_and_or_b32 v40, v27, -16, v30
	v_mad_u64_u32 v[30:31], s[6:7], v32, s89, v[18:19]
	v_and_b32_e32 v27, 7, v32
	v_mad_u64_u32 v[34:35], s[6:7], v28, s89, v[18:19]
	v_and_b32_e32 v32, 7, v28
	v_mad_u64_u32 v[38:39], s[6:7], v29, s89, v[18:19]
	v_ashrrev_i32_e32 v43, 3, v22
	ds_read2_b32 v[22:23], v24 offset1:1
	ds_read2_b32 v[24:25], v24 offset0:2 offset1:3
	v_and_b32_e32 v45, 7, v29
	ds_read2_b32 v[28:29], v30 offset1:1
	ds_read2_b32 v[30:31], v30 offset0:2 offset1:3
	v_and_or_b32 v42, v33, -16, v27
	v_and_or_b32 v44, v36, -16, v32
	ds_read2_b32 v[32:33], v34 offset1:1
	ds_read2_b32 v[34:35], v34 offset0:2 offset1:3
	ds_read2_b32 v[36:37], v38 offset1:1
	ds_read2_b32 v[38:39], v38 offset0:2 offset1:3
	v_ashrrev_i32_e32 v41, 31, v40
	v_and_or_b32 v46, v43, -16, v45
	s_addk_i32 s2, 0x100
	v_lshlrev_b64 v[40:41], 11, v[40:41]
	v_ashrrev_i32_e32 v43, 31, v42
	v_ashrrev_i32_e32 v45, 31, v44
	v_ashrrev_i32_e32 v47, 31, v46
	s_cmpk_lg_i32 s2, 0x200
	v_lshl_add_u64 v[40:41], v[0:1], 0, v[40:41]
	v_lshlrev_b64 v[42:43], 11, v[42:43]
	v_lshlrev_b64 v[44:45], 11, v[44:45]
	v_lshlrev_b64 v[46:47], 11, v[46:47]
	v_lshl_add_u64 v[42:43], v[0:1], 0, v[42:43]
	v_lshl_add_u64 v[44:45], v[0:1], 0, v[44:45]
	v_lshl_add_u64 v[46:47], v[0:1], 0, v[46:47]
	s_waitcnt lgkmcnt(6)
	global_store_dwordx4 v[40:41], v[22:25], off
	s_waitcnt lgkmcnt(4)
	global_store_dwordx4 v[42:43], v[28:31], off
	s_waitcnt lgkmcnt(2)
	global_store_dwordx4 v[44:45], v[32:35], off
	s_waitcnt lgkmcnt(0)
	global_store_dwordx4 v[46:47], v[36:39], off
	s_cbranch_scc1 .LBB0_228
	s_waitcnt lgkmcnt(0)
	s_add_i32 s4, s4, s41
	s_movk_i32 s32, 0x4c00
	s_cmpk_eq_i32 s99, 0x100
	s_cselect_b32 s32, 0x4000, s32
	s_cmp_lt_i32 s4, s32
	s_cbranch_scc1 .LBB0_227

.LBB0_236:
	v_and_b32_e32 v2, 15, v0
	v_or_b32_e32 v3, s63, v2
	v_lshlrev_b32_e32 v6, 4, v0
	v_lshlrev_b32_e32 v4, 6, v3
	v_and_b32_e32 v5, 48, v0
	s_movk_i32 s0, 0x3c0
	v_and_b32_e32 v6, 0xfffffc00, v6
	v_lshlrev_b32_e32 v3, 2, v3
	v_and_or_b32 v4, v4, s0, v5
	v_add_u32_e32 v7, s65, v6
	v_and_b32_e32 v3, 32, v3
	v_lshlrev_b32_e32 v0, 2, v0
	v_bitop3_b32 v4, v4, v7, v3 bitop3:0xde
	v_lshl_or_b32 v2, v2, 6, v5
	v_add_u32_e32 v3, s67, v6
	v_and_b32_e32 v0, 32, v0
	v_bitop3_b32 v177, v2, v3, v0 bitop3:0xde
	v_mbcnt_lo_u32_b32 v0, -1, 0
	v_mbcnt_hi_u32_b32 v0, -1, v0
	v_and_b32_e32 v5, 15, v0
	v_lshrrev_b32_e32 v0, 4, v0
	v_bfe_u32 v6, v5, 1, 3
	v_and_b32_e32 v7, 1, v6
	v_lshlrev_b32_e32 v7, 1, v7
	v_and_or_b32 v6, v6, 4, v7
	v_xor_b32_e32 v0, v0, v6
	v_lshlrev_b32_e32 v0, 4, v0
	v_lshl_add_u32 v0, v5, 7, v0
	v_add_u32_e32 v4, s65, v0
	v_xor_b32_e32 v212, 64, v4
	v_add_u32_e32 v177, s67, v0
	v_xor_b32_e32 v213, 64, v177
	v_add_u32_e32 v213, 0x10000, v213
	s_waitcnt vmcnt(2)
	s_barrier
	s_add_i32 m0, s97, 0x18000
	v_lshl_add_u64 v[2:3], s[6:7], 0, v[160:161]
	v_lshl_add_u64 v[2:3], v[2:3], 0, s[52:53]
	global_load_lds_dwordx4 v[2:3], off
	v_mov_b32_e32 v163, v161
	s_add_i32 m0, s97, 0x1a000
	s_add_u32 s0, s70, 0x32000080
	v_lshl_add_u64 v[2:3], s[6:7], 0, v[162:163]
	v_lshl_add_u64 v[2:3], v[2:3], 0, s[52:53]
	s_addc_u32 s1, s71, 0
	s_add_i32 s31, s97, 0x8000
	global_load_lds_dwordx4 v[2:3], off
	s_mov_b32 m0, s31
	s_add_i32 s42, s97, 0xa000
	v_mov_b32_e32 v0, 0
	global_load_lds_dwordx4 v164, s[0:1]
	s_mov_b32 m0, s42
	s_mov_b32 s47, 0
	global_load_lds_dwordx4 v166, s[0:1]
	s_add_u32 s0, s6, 0x8080
	s_addc_u32 s1, s7, 0
	s_add_i32 m0, s97, 0x1c000
	v_add_u32_e32 v178, 0, v4
	global_load_lds_dwordx4 v160, s[0:1]
	s_add_i32 m0, s97, 0x1e000
	v_mov_b32_e32 v168, v160
	global_load_lds_dwordx4 v162, s[0:1]
	s_waitcnt vmcnt(6)
	v_mov_b32_e32 v160, v1
	s_mov_b32 s43, s82
	s_mov_b32 s83, s44
	v_mov_b32_e32 v1, v0
	v_mov_b32_e32 v2, v0
	v_mov_b32_e32 v3, v0
	v_mov_b32_e32 v4, v0
	v_mov_b32_e32 v5, v0
	v_mov_b32_e32 v6, v0
	v_mov_b32_e32 v7, v0
	v_mov_b32_e32 v8, v0
	v_mov_b32_e32 v9, v0
	v_mov_b32_e32 v10, v0
	v_mov_b32_e32 v11, v0
	v_mov_b32_e32 v12, v0
	v_mov_b32_e32 v13, v0
	v_mov_b32_e32 v14, v0
	v_mov_b32_e32 v15, v0
	v_mov_b32_e32 v16, v0
	v_mov_b32_e32 v17, v0
	v_mov_b32_e32 v18, v0
	v_mov_b32_e32 v19, v0
	v_mov_b32_e32 v20, v0
	v_mov_b32_e32 v21, v0
	v_mov_b32_e32 v22, v0
	v_mov_b32_e32 v23, v0
	v_mov_b32_e32 v24, v0
	v_mov_b32_e32 v25, v0
	v_mov_b32_e32 v26, v0
	v_mov_b32_e32 v27, v0
	v_mov_b32_e32 v28, v0
	v_mov_b32_e32 v29, v0
	v_mov_b32_e32 v30, v0
	v_mov_b32_e32 v31, v0
	v_mov_b32_e32 v36, v0
	v_mov_b32_e32 v37, v0
	v_mov_b32_e32 v38, v0
	v_mov_b32_e32 v39, v0
	v_mov_b32_e32 v44, v0
	v_mov_b32_e32 v45, v0
	v_mov_b32_e32 v46, v0
	v_mov_b32_e32 v47, v0
	v_mov_b32_e32 v32, v0
	v_mov_b32_e32 v33, v0
	v_mov_b32_e32 v34, v0
	v_mov_b32_e32 v35, v0
	v_mov_b32_e32 v40, v0
	v_mov_b32_e32 v41, v0
	v_mov_b32_e32 v42, v0
	v_mov_b32_e32 v43, v0
	v_mov_b32_e32 v48, v0
	v_mov_b32_e32 v49, v0
	v_mov_b32_e32 v50, v0
	v_mov_b32_e32 v51, v0
	v_mov_b32_e32 v52, v0
	v_mov_b32_e32 v53, v0
	v_mov_b32_e32 v54, v0
	v_mov_b32_e32 v55, v0
	v_mov_b32_e32 v56, v0
	v_mov_b32_e32 v57, v0
	v_mov_b32_e32 v58, v0
	v_mov_b32_e32 v59, v0
	v_mov_b32_e32 v60, v0
	v_mov_b32_e32 v61, v0
	v_mov_b32_e32 v62, v0
	v_mov_b32_e32 v63, v0
	v_mov_b32_e32 v64, v0
	v_mov_b32_e32 v65, v0
	v_mov_b32_e32 v66, v0
	v_mov_b32_e32 v67, v0
	v_mov_b32_e32 v68, v0
	v_mov_b32_e32 v69, v0
	v_mov_b32_e32 v70, v0
	v_mov_b32_e32 v71, v0
	v_mov_b32_e32 v72, v0
	v_mov_b32_e32 v73, v0
	v_mov_b32_e32 v74, v0
	v_mov_b32_e32 v75, v0
	v_mov_b32_e32 v76, v0
	v_mov_b32_e32 v77, v0
	v_mov_b32_e32 v78, v0
	v_mov_b32_e32 v79, v0
	v_mov_b32_e32 v80, v0
	v_mov_b32_e32 v81, v0
	v_mov_b32_e32 v82, v0
	v_mov_b32_e32 v83, v0
	v_mov_b32_e32 v84, v0
	v_mov_b32_e32 v85, v0
	v_mov_b32_e32 v86, v0
	v_mov_b32_e32 v87, v0
	v_mov_b32_e32 v88, v0
	v_mov_b32_e32 v89, v0
	v_mov_b32_e32 v90, v0
	v_mov_b32_e32 v91, v0
	v_mov_b32_e32 v92, v0
	v_mov_b32_e32 v93, v0
	v_mov_b32_e32 v94, v0
	v_mov_b32_e32 v95, v0
	v_mov_b32_e32 v96, v0
	v_mov_b32_e32 v97, v0
	v_mov_b32_e32 v98, v0
	v_mov_b32_e32 v99, v0
	v_mov_b32_e32 v100, v0
	v_mov_b32_e32 v101, v0
	v_mov_b32_e32 v102, v0
	v_mov_b32_e32 v103, v0
	v_mov_b32_e32 v104, v0
	v_mov_b32_e32 v105, v0
	v_mov_b32_e32 v106, v0
	v_mov_b32_e32 v107, v0
	v_mov_b32_e32 v108, v0
	v_mov_b32_e32 v109, v0
	v_mov_b32_e32 v110, v0
	v_mov_b32_e32 v111, v0
	v_mov_b32_e32 v112, v0
	v_mov_b32_e32 v113, v0
	v_mov_b32_e32 v114, v0
	v_mov_b32_e32 v115, v0
	v_mov_b32_e32 v116, v0
	v_mov_b32_e32 v117, v0
	v_mov_b32_e32 v118, v0
	v_mov_b32_e32 v119, v0
	v_mov_b32_e32 v120, v0
	v_mov_b32_e32 v121, v0
	v_mov_b32_e32 v122, v0
	v_mov_b32_e32 v123, v0
	v_mov_b32_e32 v124, v0
	v_mov_b32_e32 v125, v0
	v_mov_b32_e32 v126, v0
	v_mov_b32_e32 v127, v0
	v_mbcnt_lo_u32_b32 v244, -1, 0
	v_mbcnt_hi_u32_b32 v244, -1, v244
	v_lshrrev_b32_e32 v245, 3, v244
	v_and_b32_e32 v246, 7, v244
	v_lshlrev_b32_e32 v248, 17, v245
	v_lshl_or_b32 v248, v246, 4, v248
	v_lshrrev_b32_e32 v247, 1, v246
	v_and_b32_e32 v246, 1, v246
	v_lshlrev_b32_e32 v249, 15, v247
	v_lshl_or_b32 v249, v246, 13, v249
	v_lshl_or_b32 v249, v245, 3, v249
	v_mov_b32_e32 v252, 0x43800000
	v_mov_b32_e32 v253, 0x43800000
	v_readlane_b32 s32, v255, 54
	s_nop 0
	v_mov_b32_e32 v250, s32
	v_readlane_b32 s32, v255, 55
	s_nop 0
	v_mov_b32_e32 v251, s32
	s_barrier

.LBB0_247:
	s_min_i32 s0, s47, s88
	s_mul_i32 s0, s0, s41
	s_add_i32 s0, s0, s59
	s_min_i32 s24, s0, 0x2fff
	v_readlane_b32 s0, v254, 13
	v_readlane_b32 s1, v254, 14
	v_mbcnt_lo_u32_b32 v128, -1, 0
	v_mbcnt_hi_u32_b32 v128, -1, v128
	v_readlane_b32 s0, v255, 54
	v_readlane_b32 s1, v255, 55
	s_ashr_i32 s6, s24, 12
	s_add_i32 s80, s6, 21
	s_ashr_i32 s81, s80, 31
	s_lshl_b64 s[6:7], s[80:81], 25
	s_waitcnt lgkmcnt(0)
	s_add_u32 s0, s0, s6
	s_addc_u32 s1, s1, s7
	s_lshr_b32 s6, s24, 1
	s_and_b32 s8, s6, 0x7c0
	v_and_b32_e32 v129, 0xffff8, v128
	s_lshl_b32 s6, s24, 5
	v_lshlrev_b32_e32 v128, 2, v128
	v_add_lshl_u32 v129, v129, s8, 12
	s_and_b32 s6, s6, 0xfe0
	v_and_b32_e32 v128, 28, v128
	v_or3_b32 v128, v129, s6, v128
	v_mov_b32_e32 v129, v161
	v_lshl_add_u64 v[152:153], v[128:129], 2, s[0:1]
	v_add_co_u32_e32 v132, vcc, s90, v152
	s_nop 1
	v_addc_co_u32_e32 v133, vcc, 0, v153, vcc
	v_add_co_u32_e32 v136, vcc, s91, v152
	global_load_dwordx4 v[128:131], v[152:153], off nt
	s_nop 0
	global_load_dwordx4 v[132:135], v[132:133], off nt
	v_addc_co_u32_e32 v137, vcc, 0, v153, vcc
	v_add_co_u32_e32 v140, vcc, s92, v152
	s_nop 1
	v_addc_co_u32_e32 v141, vcc, 0, v153, vcc
	v_add_co_u32_e32 v144, vcc, s93, v152
	global_load_dwordx4 v[136:139], v[136:137], off nt
	s_nop 0
	global_load_dwordx4 v[140:143], v[140:141], off nt
	v_addc_co_u32_e32 v145, vcc, 0, v153, vcc
	v_add_co_u32_e32 v148, vcc, 0x14000, v152
	s_nop 1
	v_addc_co_u32_e32 v149, vcc, 0, v153, vcc
	v_add_co_u32_e32 v154, vcc, 0x18000, v152
	global_load_dwordx4 v[144:147], v[144:145], off nt
	s_nop 0
	global_load_dwordx4 v[148:151], v[148:149], off nt
	v_addc_co_u32_e32 v155, vcc, 0, v153, vcc
	v_add_co_u32_e32 v156, vcc, 0x1c000, v152
	s_nop 1
	v_addc_co_u32_e32 v157, vcc, 0, v153, vcc
	global_load_dwordx4 v[152:155], v[154:155], off nt
	s_nop 0
	global_load_dwordx4 v[156:159], v[156:157], off nt
	s_add_i32 s32, s47, 6
	s_mul_i32 s32, s32, s41
	s_add_i32 s32, s32, s59
	s_min_u32 s32, s32, 0x5fff
	v_mov_b32_e32 v214, s32
	v_lshrrev_b32_e32 v215, 12, v214
	v_add_u32_e32 v215, 13, v215
	v_lshlrev_b32_e32 v215, 25, v215
	v_bfe_u32 v216, v214, 7, 5
	v_lshl_or_b32 v215, v216, 20, v215
	v_and_b32_e32 v216, 0x7f, v214
	v_lshl_or_b32 v215, v216, 7, v215
	v_or_b32_e32 v216, v215, v248
	v_mov_b32_e32 v217, 0
	v_lshl_add_u64 v[218:219], v[216:217], 0, v[250:251]
	global_load_dwordx4 v[188:191], v[218:219], off nt
	v_add_u32_e32 v216, 0x4000, v216
	v_lshl_add_u64 v[218:219], v[216:217], 0, v[250:251]
	global_load_dwordx4 v[192:195], v[218:219], off nt
	v_add_u32_e32 v216, 0x4000, v216
	v_lshl_add_u64 v[218:219], v[216:217], 0, v[250:251]
	global_load_dwordx4 v[196:199], v[218:219], off nt
	v_add_u32_e32 v216, 0x4000, v216
	v_lshl_add_u64 v[218:219], v[216:217], 0, v[250:251]
	global_load_dwordx4 v[200:203], v[218:219], off nt
	v_add_u32_e32 v216, 0x4000, v216
	v_lshl_add_u64 v[218:219], v[216:217], 0, v[250:251]
	global_load_dwordx4 v[204:207], v[218:219], off nt
	v_add_u32_e32 v216, 0x4000, v216
	v_lshl_add_u64 v[218:219], v[216:217], 0, v[250:251]
	global_load_dwordx4 v[208:211], v[218:219], off nt
	v_add_u32_e32 v216, 0x4000, v216
	v_lshl_add_u64 v[218:219], v[216:217], 0, v[250:251]
	global_load_dwordx4 v[240:243], v[218:219], off nt
	v_add_u32_e32 v216, 0x4000, v216
	v_lshl_add_u64 v[218:219], v[216:217], 0, v[250:251]
	global_load_dwordx4 v[244:247], v[218:219], off nt
	s_and_b64 vcc, exec, s[20:21]
	s_cbranch_vccz .LBB0_249
	s_barrier

.LBB0_281:
	v_cvt_pk_bf16_f32 v180, v163, v165
	v_cvt_pk_bf16_f32 v181, v167, v169
	s_nop 0
	v_cvt_pk_bf16_f32 v182, v171, v174
	v_cvt_pk_bf16_f32 v183, v175, v179
	global_store_dwordx4 v[172:173], v[180:183], off offset:16
	s_add_u32 s0, s75, 0xffffff00
	s_addc_u32 s1, s48, -1
	s_waitcnt vmcnt(16)
	v_mul_f32_e32 v128, 0x43800000, v128
	v_mul_f32_e32 v132, 0x43800000, v132
	v_mov_b32_e32 v180, v161
	v_cvt_pk_fp8_f32 v180, v128, v132
	v_mul_f32_e32 v128, 0x43800000, v144
	v_mul_f32_e32 v132, 0x43800000, v148
	v_mov_b32_e32 v181, v161
	v_cvt_pk_fp8_f32 v181, v128, v132
	v_mul_f32_e32 v128, 0x43800000, v152
	v_mul_f32_e32 v132, 0x43800000, v156
	v_mul_f32_e32 v129, 0x43800000, v129
	v_cvt_pk_fp8_f32 v181, v128, v132 op_sel:[0,0,1]
	v_mul_f32_e32 v132, 0x43800000, v133
	v_mov_b32_e32 v128, v161
	v_mul_f32_e32 v133, 0x43800000, v137
	v_cvt_pk_fp8_f32 v128, v129, v132
	v_mul_f32_e32 v132, 0x43800000, v145
	v_mul_f32_e32 v137, 0x43800000, v149
	v_mov_b32_e32 v129, v161
	v_cvt_pk_fp8_f32 v129, v132, v137
	v_mul_f32_e32 v136, 0x43800000, v136
	v_mul_f32_e32 v140, 0x43800000, v140
	v_cvt_pk_fp8_f32 v180, v136, v140 op_sel:[0,0,1]
	v_mul_f32_e32 v136, 0x43800000, v141
	v_cvt_pk_fp8_f32 v128, v133, v136 op_sel:[0,0,1]
	v_mul_f32_e32 v132, 0x43800000, v153
	v_mul_f32_e32 v133, 0x43800000, v157
	s_lshl_b32 s6, s24, 6
	s_lshr_b32 s7, s24, 3
	v_cvt_pk_fp8_f32 v129, v132, v133 op_sel:[0,0,1]
	v_mul_f32_e32 v130, 0x43800000, v130
	v_mul_f32_e32 v133, 0x43800000, v134
	v_mov_b32_e32 v132, v161
	s_and_b32 s6, s6, 0xfc0
	s_and_b32 s7, s7, 8
	v_cvt_pk_fp8_f32 v132, v130, v133
	v_mul_f32_e32 v130, 0x43800000, v146
	v_mul_f32_e32 v137, 0x43800000, v150
	v_mov_b32_e32 v133, v161
	s_or_b32 s34, s6, s7
	v_readlane_b32 s6, v254, 13
	v_cvt_pk_fp8_f32 v133, v130, v137
	v_readlane_b32 s7, v254, 14
	v_mbcnt_lo_u32_b32 v163, -1, 0
	v_mbcnt_hi_u32_b32 v163, -1, v163
	v_mul_f32_e32 v134, 0x43800000, v138
	v_mul_f32_e32 v136, 0x43800000, v142
	s_mov_b64 s[6:7], s[100:101]
	v_cvt_pk_fp8_f32 v132, v134, v136 op_sel:[0,0,1]
	v_mul_f32_e32 v130, 0x43800000, v154
	v_mul_f32_e32 v134, 0x43800000, v158
	s_lshl_b64 s[24:25], s[80:81], 12
	v_lshlrev_b32_e32 v165, 3, v163
	v_lshlrev_b32_e32 v167, 2, v163
	v_cvt_pk_fp8_f32 v133, v130, v134 op_sel:[0,0,1]
	v_mul_f32_e32 v131, 0x43800000, v131
	v_mul_f32_e32 v134, 0x43800000, v135
	v_mov_b32_e32 v130, v161
	s_or_b32 s24, s24, s34
	v_and_b32_e32 v165, 48, v165
	v_and_b32_e32 v167, 4, v167
	v_cvt_pk_fp8_f32 v130, v131, v134
	v_mul_f32_e32 v134, 0x43800000, v147
	v_mul_f32_e32 v137, 0x43800000, v151
	v_mov_b32_e32 v131, v161
	v_or3_b32 v172, s24, v165, v167
	v_mov_b32_e32 v173, s25
	v_cvt_pk_fp8_f32 v131, v134, v137
	v_lshlrev_b64 v[172:173], 11, v[172:173]
	s_waitcnt lgkmcnt(0)
	v_lshl_add_u64 v[172:173], s[6:7], 0, v[172:173]
	v_and_b32_e32 v174, -8, v163
	v_mul_f32_e32 v135, 0x43800000, v139
	v_mul_f32_e32 v136, 0x43800000, v143
	v_lshl_add_u64 v[172:173], v[172:173], 0, s[8:9]
	v_ashrrev_i32_e32 v175, 31, v174
	v_cvt_pk_fp8_f32 v130, v135, v136 op_sel:[0,0,1]
	v_mul_f32_e32 v134, 0x43800000, v155
	v_mul_f32_e32 v135, 0x43800000, v159
	v_lshl_add_u64 v[172:173], v[172:173], 0, v[174:175]
	v_cvt_pk_fp8_f32 v131, v134, v135 op_sel:[0,0,1]
	v_lshl_add_u64 v[174:175], v[172:173], 0, s[12:13]
	v_add_co_u32_e32 v172, vcc, s95, v172
	s_nop 1
	v_addc_co_u32_e32 v173, vcc, 0, v173, vcc
	s_and_b64 vcc, exec, s[4:5]
	global_store_dwordx2 v[172:173], v[180:181], off offset:-4096
	global_store_dwordx2 v[174:175], v[128:129], off offset:2048
	global_store_dwordx2 v[172:173], v[132:133], off
	global_store_dwordx2 v[172:173], v[130:131], off offset:2048
	s_add_i32 s32, s47, 6
	s_mul_i32 s32, s32, s41
	s_add_i32 s32, s32, s59
	s_min_u32 s32, s32, 0x5fff
	s_waitcnt vmcnt(20)
	v_mov_b32_e32 v214, s32
	v_lshrrev_b32_e32 v215, 12, v214
	v_add_u32_e32 v215, 13, v215
	v_lshlrev_b32_e32 v215, 23, v215
	v_bfe_u32 v216, v214, 2, 4
	v_lshl_or_b32 v215, v216, 19, v215
	v_and_b32_e32 v216, 3, v214
	v_lshl_or_b32 v215, v216, 17, v215
	v_bfe_u32 v216, v214, 6, 1
	v_lshl_or_b32 v215, v216, 14, v215
	v_bfe_u32 v216, v214, 7, 5
	v_lshl_or_b32 v215, v216, 6, v215
	v_or_b32_e32 v215, v215, v249
	v_add_u32_e32 v215, 0x2000000, v215
	v_add_u32_e32 v216, 0x1000, v215
	v_pk_mul_f32 v[188:189], v[188:189], v[252:253]
	v_pk_mul_f32 v[190:191], v[190:191], v[252:253]
	v_pk_mul_f32 v[192:193], v[192:193], v[252:253]
	v_pk_mul_f32 v[194:195], v[194:195], v[252:253]
	v_pk_mul_f32 v[196:197], v[196:197], v[252:253]
	v_pk_mul_f32 v[198:199], v[198:199], v[252:253]
	v_pk_mul_f32 v[200:201], v[200:201], v[252:253]
	v_pk_mul_f32 v[202:203], v[202:203], v[252:253]
	v_pk_mul_f32 v[204:205], v[204:205], v[252:253]
	v_pk_mul_f32 v[206:207], v[206:207], v[252:253]
	v_pk_mul_f32 v[208:209], v[208:209], v[252:253]
	v_pk_mul_f32 v[210:211], v[210:211], v[252:253]
	v_pk_mul_f32 v[240:241], v[240:241], v[252:253]
	v_pk_mul_f32 v[242:243], v[242:243], v[252:253]
	v_pk_mul_f32 v[244:245], v[244:245], v[252:253]
	v_pk_mul_f32 v[246:247], v[246:247], v[252:253]
	v_cvt_pk_fp8_f32 v220, v188, v192
	v_cvt_pk_fp8_f32 v221, v204, v208
	v_cvt_pk_fp8_f32 v222, v189, v193
	v_cvt_pk_fp8_f32 v223, v205, v209
	v_cvt_pk_fp8_f32 v224, v190, v194
	v_cvt_pk_fp8_f32 v225, v206, v210
	v_cvt_pk_fp8_f32 v226, v191, v195
	v_cvt_pk_fp8_f32 v227, v207, v211
	v_cvt_pk_fp8_f32 v220, v196, v200 op_sel:[0,0,1]
	v_cvt_pk_fp8_f32 v221, v240, v244 op_sel:[0,0,1]
	v_cvt_pk_fp8_f32 v222, v197, v201 op_sel:[0,0,1]
	v_cvt_pk_fp8_f32 v223, v241, v245 op_sel:[0,0,1]
	v_cvt_pk_fp8_f32 v224, v198, v202 op_sel:[0,0,1]
	v_cvt_pk_fp8_f32 v225, v242, v246 op_sel:[0,0,1]
	v_cvt_pk_fp8_f32 v226, v199, v203 op_sel:[0,0,1]
	v_cvt_pk_fp8_f32 v227, v243, v247 op_sel:[0,0,1]
	global_store_dwordx2 v215, v[220:221], s[100:101]
	global_store_dwordx2 v215, v[222:223], s[100:101] offset:2048
	global_store_dwordx2 v216, v[224:225], s[100:101]
	global_store_dwordx2 v216, v[226:227], s[100:101] offset:2048
	s_cbranch_vccnz .LBB0_285
	s_and_b64 vcc, exec, s[2:3]
	s_cbranch_vccnz .LBB0_284
	s_barrier
